# final LayerNorm phase: the f32 output rows are stored non-temporal (written once, never re-read) so they do not displace the y2/h2 rows still to be read from the memory-side cache
# speedup vs baseline: 1.0098x; 1.0098x over previous
; __device__ __forceinline__ float bflo(unsigned w) { return __uint_as_float(w << 16); }
; __device__ __forceinline__ float bfhi(unsigned w) { return __uint_as_float(w & 0xffff0000u); }
; __device__ __forceinline__ void ph_ln3(const Params& p) {
;     ...
;         const float g0 = gates[row * 2], g1 = gates[row * 2 + 1], m2 = stats2[row * 2], r2 = stats2[row * 2 + 1] * ALPHA; f32x4 v[8];
; #pragma unroll
;         for (int j = 0; j < 8; ++j) { const f32x4 a = (f32x4){bflo(na[j].x), bfhi(na[j].x), bflo(na[j].y), bfhi(na[j].y)}, b = (f32x4){bflo(nb[j].x), bfhi(nb[j].x), bflo(nb[j].y), bfhi(nb[j].y)};
;             const f32x4 gg = *(const f32x4*)(p.ln2_g + j * 256 + lane * 4), bb = *(const f32x4*)(p.ln2_b + j * 256 + lane * 4);
;             v[j] = (((f32x4){bflo(nh[j].x), bfhi(nh[j].x), bflo(nh[j].y), bfhi(nh[j].y)} - m2) * r2) * gg + bb * ALPHA + (a * g0 + b * g1); }
.LBB0_1509:
	s_or_b64 exec, exec, s[10:11]
	s_waitcnt vmcnt(16)
	v_mul_f32_e32 v214, 0x3f9837f0, v189
	v_lshlrev_b32_e32 v111, 16, v208
	v_and_b32_e32 v189, 0xffff0000, v208
	v_lshlrev_b32_e32 v208, 16, v209
	v_and_b32_e32 v209, 0xffff0000, v209
	v_sub_f32_e32 v209, v209, v185
	v_sub_f32_e32 v208, v208, v185
	v_sub_f32_e32 v221, v189, v185
	v_sub_f32_e32 v220, v111, v185
	v_pk_mul_f32 v[220:221], v[220:221], v[214:215] op_sel_hi:[1,0]
	v_pk_mul_f32 v[208:209], v[208:209], v[214:215] op_sel_hi:[1,0]
	v_lshlrev_b32_e32 v218, 16, v212
	v_and_b32_e32 v219, 0xffff0000, v212
	v_lshlrev_b32_e32 v212, 16, v213
	v_and_b32_e32 v213, 0xffff0000, v213
	s_waitcnt vmcnt(15)
	v_pk_mul_f32 v[62:63], v[62:63], v[208:209]
	v_pk_mul_f32 v[60:61], v[60:61], v[220:221]
	v_lshlrev_b32_e32 v216, 16, v210
	v_and_b32_e32 v217, 0xffff0000, v210
	v_lshlrev_b32_e32 v210, 16, v211
	v_and_b32_e32 v211, 0xffff0000, v211
	s_waitcnt vmcnt(13)
	v_pk_fma_f32 v[60:61], v[56:57], s[8:9], v[60:61] op_sel_hi:[1,0,1]
	v_pk_fma_f32 v[56:57], v[58:59], s[8:9], v[62:63] op_sel_hi:[1,0,1]
	v_pk_mul_f32 v[58:59], v[188:189], v[212:213] op_sel_hi:[0,1]
	v_pk_mul_f32 v[62:63], v[188:189], v[218:219] op_sel_hi:[0,1]
	v_lshlrev_b32_e32 v111, 16, v202
	v_and_b32_e32 v189, 0xffff0000, v202
	v_lshlrev_b32_e32 v202, 16, v203
	v_and_b32_e32 v203, 0xffff0000, v203
	v_pk_fma_f32 v[62:63], v[184:185], v[216:217], v[62:63] op_sel_hi:[0,1,1]
	v_pk_fma_f32 v[58:59], v[184:185], v[210:211], v[58:59] op_sel_hi:[0,1,1]
	v_sub_f32_e32 v203, v203, v185
	v_sub_f32_e32 v202, v202, v185
	v_sub_f32_e32 v209, v189, v185
	v_sub_f32_e32 v208, v111, v185
	v_pk_add_f32 v[56:57], v[58:59], v[56:57]
	v_pk_add_f32 v[58:59], v[62:63], v[60:61]
	v_lshlrev_b32_e32 v60, 16, v204
	v_and_b32_e32 v61, 0xffff0000, v204
	v_lshlrev_b32_e32 v62, 16, v205
	v_and_b32_e32 v63, 0xffff0000, v205
	v_lshlrev_b32_e32 v204, 16, v206
	v_and_b32_e32 v205, 0xffff0000, v206
	v_lshlrev_b32_e32 v206, 16, v207
	v_and_b32_e32 v207, 0xffff0000, v207
	v_pk_mul_f32 v[208:209], v[208:209], v[214:215] op_sel_hi:[1,0]
	v_pk_mul_f32 v[202:203], v[202:203], v[214:215] op_sel_hi:[1,0]
	s_waitcnt vmcnt(12)
	v_pk_mul_f32 v[54:55], v[54:55], s[8:9] op_sel_hi:[1,0]
	v_pk_mul_f32 v[52:53], v[52:53], s[8:9] op_sel_hi:[1,0]
	v_pk_fma_f32 v[50:51], v[202:203], v[50:51], v[54:55]
	v_pk_fma_f32 v[52:53], v[208:209], v[48:49], v[52:53]
	v_pk_mul_f32 v[48:49], v[188:189], v[206:207] op_sel_hi:[0,1]
	v_pk_mul_f32 v[54:55], v[188:189], v[204:205] op_sel_hi:[0,1]
	v_pk_fma_f32 v[54:55], v[184:185], v[60:61], v[54:55] op_sel_hi:[0,1,1]
	v_pk_fma_f32 v[48:49], v[184:185], v[62:63], v[48:49] op_sel_hi:[0,1,1]
	v_lshlrev_b32_e32 v111, 16, v196
	v_and_b32_e32 v189, 0xffff0000, v196
	v_lshlrev_b32_e32 v196, 16, v197
	v_and_b32_e32 v197, 0xffff0000, v197
	v_pk_add_f32 v[48:49], v[48:49], v[50:51]
	v_pk_add_f32 v[50:51], v[54:55], v[52:53]
	v_lshlrev_b32_e32 v52, 16, v198
	v_and_b32_e32 v53, 0xffff0000, v198
	v_lshlrev_b32_e32 v54, 16, v199
	v_and_b32_e32 v55, 0xffff0000, v199
	v_sub_f32_e32 v197, v197, v185
	v_sub_f32_e32 v196, v196, v185
	v_sub_f32_e32 v199, v189, v185
	v_sub_f32_e32 v198, v111, v185
	v_lshlrev_b32_e32 v60, 16, v200
	v_and_b32_e32 v61, 0xffff0000, v200
	v_lshlrev_b32_e32 v62, 16, v201
	v_and_b32_e32 v63, 0xffff0000, v201
	v_pk_mul_f32 v[198:199], v[198:199], v[214:215] op_sel_hi:[1,0]
	v_pk_mul_f32 v[196:197], v[196:197], v[214:215] op_sel_hi:[1,0]
	s_waitcnt vmcnt(9)
	v_pk_mul_f32 v[46:47], v[46:47], s[8:9] op_sel_hi:[1,0]
	v_pk_mul_f32 v[44:45], v[44:45], s[8:9] op_sel_hi:[1,0]
	v_pk_fma_f32 v[42:43], v[196:197], v[42:43], v[46:47]
	v_pk_fma_f32 v[44:45], v[198:199], v[40:41], v[44:45]
	v_pk_mul_f32 v[40:41], v[188:189], v[62:63] op_sel_hi:[0,1]
	v_pk_mul_f32 v[46:47], v[188:189], v[60:61] op_sel_hi:[0,1]
	v_lshlrev_b32_e32 v62, 16, v190
	v_and_b32_e32 v63, 0xffff0000, v190
	v_lshlrev_b32_e32 v60, 16, v191
	v_and_b32_e32 v61, 0xffff0000, v191
	v_sub_f32_e32 v61, v61, v185
	v_sub_f32_e32 v60, v60, v185
	v_sub_f32_e32 v63, v63, v185
	v_sub_f32_e32 v62, v62, v185
	v_pk_fma_f32 v[46:47], v[184:185], v[52:53], v[46:47] op_sel_hi:[0,1,1]
	v_pk_fma_f32 v[40:41], v[184:185], v[54:55], v[40:41] op_sel_hi:[0,1,1]
	v_lshlrev_b32_e32 v52, 16, v194
	v_and_b32_e32 v53, 0xffff0000, v194
	v_lshlrev_b32_e32 v54, 16, v195
	v_and_b32_e32 v55, 0xffff0000, v195
	v_pk_mul_f32 v[62:63], v[62:63], v[214:215] op_sel_hi:[1,0]
	v_pk_mul_f32 v[60:61], v[60:61], v[214:215] op_sel_hi:[1,0]
	s_waitcnt vmcnt(8)
	v_pk_mul_f32 v[38:39], v[38:39], s[8:9] op_sel_hi:[1,0]
	v_pk_mul_f32 v[36:37], v[36:37], s[8:9] op_sel_hi:[1,0]
	v_pk_fma_f32 v[34:35], v[60:61], v[34:35], v[38:39]
	v_pk_fma_f32 v[36:37], v[62:63], v[32:33], v[36:37]
	v_pk_mul_f32 v[32:33], v[188:189], v[54:55] op_sel_hi:[0,1]
	v_pk_mul_f32 v[38:39], v[188:189], v[52:53] op_sel_hi:[0,1]
	v_lshlrev_b32_e32 v54, 16, v180
	v_and_b32_e32 v55, 0xffff0000, v180
	v_lshlrev_b32_e32 v52, 16, v181
	v_and_b32_e32 v53, 0xffff0000, v181
	v_pk_add_f32 v[40:41], v[40:41], v[42:43]
	v_pk_add_f32 v[42:43], v[46:47], v[44:45]
	v_lshlrev_b32_e32 v44, 16, v192
	v_and_b32_e32 v45, 0xffff0000, v192
	v_lshlrev_b32_e32 v46, 16, v193
	v_and_b32_e32 v47, 0xffff0000, v193
	v_sub_f32_e32 v53, v53, v185
	v_sub_f32_e32 v52, v52, v185
	v_sub_f32_e32 v55, v55, v185
	v_sub_f32_e32 v54, v54, v185
	v_pk_fma_f32 v[38:39], v[184:185], v[44:45], v[38:39] op_sel_hi:[0,1,1]
	v_pk_fma_f32 v[32:33], v[184:185], v[46:47], v[32:33] op_sel_hi:[0,1,1]
	v_lshlrev_b32_e32 v44, 16, v186
	v_and_b32_e32 v45, 0xffff0000, v186
	v_lshlrev_b32_e32 v46, 16, v187
	v_and_b32_e32 v47, 0xffff0000, v187
	v_pk_mul_f32 v[54:55], v[54:55], v[214:215] op_sel_hi:[1,0]
	v_pk_mul_f32 v[52:53], v[52:53], v[214:215] op_sel_hi:[1,0]
	s_waitcnt vmcnt(6)
; __device__ __forceinline__ float bflo(unsigned w) { return __uint_as_float(w << 16); }
; __device__ __forceinline__ float bfhi(unsigned w) { return __uint_as_float(w & 0xffff0000u); }
; __device__ __forceinline__ void ln_row(f32x4 (&v)[8], const float* g, const float* b, int lane) {
;     ...
;     for (int j = 0; j < 8; ++j) s += (v[j][0] + v[j][1]) + (v[j][2] + v[j][3]);
;     const float mean = wave_sum(s) * (1.0f / DM); float q = 0.f;
; __device__ __forceinline__ void ph_ln3(const Params& p) {
;     ...
;         for (int j = 0; j < 8; ++j) { const f32x4 a = (f32x4){bflo(na[j].x), bfhi(na[j].x), bflo(na[j].y), bfhi(na[j].y)}, b = (f32x4){bflo(nb[j].x), bfhi(nb[j].x), bflo(nb[j].y), bfhi(nb[j].y)};
;             const f32x4 gg = *(const f32x4*)(p.ln2_g + j * 256 + lane * 4), bb = *(const f32x4*)(p.ln2_b + j * 256 + lane * 4);
;             v[j] = (((f32x4){bflo(nh[j].x), bfhi(nh[j].x), bflo(nh[j].y), bfhi(nh[j].y)} - m2) * r2) * gg + bb * ALPHA + (a * g0 + b * g1); }
	v_pk_mul_f32 v[30:31], v[30:31], s[8:9] op_sel_hi:[1,0]
	v_pk_mul_f32 v[28:29], v[28:29], s[8:9] op_sel_hi:[1,0]
	v_pk_fma_f32 v[26:27], v[52:53], v[26:27], v[30:31]
	v_pk_fma_f32 v[28:29], v[54:55], v[24:25], v[28:29]
	v_pk_mul_f32 v[24:25], v[188:189], v[46:47] op_sel_hi:[0,1]
	v_pk_mul_f32 v[30:31], v[188:189], v[44:45] op_sel_hi:[0,1]
	v_lshlrev_b32_e32 v46, 16, v174
	v_and_b32_e32 v47, 0xffff0000, v174
	v_lshlrev_b32_e32 v44, 16, v175
	v_and_b32_e32 v45, 0xffff0000, v175
	v_pk_add_f32 v[32:33], v[32:33], v[34:35]
	v_pk_add_f32 v[34:35], v[38:39], v[36:37]
	v_lshlrev_b32_e32 v36, 16, v182
	v_and_b32_e32 v37, 0xffff0000, v182
	v_lshlrev_b32_e32 v38, 16, v183
	v_and_b32_e32 v39, 0xffff0000, v183
	v_sub_f32_e32 v45, v45, v185
	v_sub_f32_e32 v44, v44, v185
	v_sub_f32_e32 v47, v47, v185
	v_sub_f32_e32 v46, v46, v185
	v_pk_fma_f32 v[30:31], v[184:185], v[36:37], v[30:31] op_sel_hi:[0,1,1]
	v_pk_fma_f32 v[24:25], v[184:185], v[38:39], v[24:25] op_sel_hi:[0,1,1]
	v_lshlrev_b32_e32 v36, 16, v178
	v_and_b32_e32 v37, 0xffff0000, v178
	v_lshlrev_b32_e32 v38, 16, v179
	v_and_b32_e32 v39, 0xffff0000, v179
	v_pk_mul_f32 v[46:47], v[46:47], v[214:215] op_sel_hi:[1,0]
	v_pk_mul_f32 v[44:45], v[44:45], v[214:215] op_sel_hi:[1,0]
	s_waitcnt vmcnt(4)
	v_pk_mul_f32 v[22:23], v[22:23], s[8:9] op_sel_hi:[1,0]
	v_pk_mul_f32 v[20:21], v[20:21], s[8:9] op_sel_hi:[1,0]
	v_pk_fma_f32 v[18:19], v[44:45], v[18:19], v[22:23]
	v_pk_fma_f32 v[20:21], v[46:47], v[16:17], v[20:21]
	v_pk_mul_f32 v[16:17], v[188:189], v[38:39] op_sel_hi:[0,1]
	v_pk_mul_f32 v[22:23], v[188:189], v[36:37] op_sel_hi:[0,1]
	v_lshlrev_b32_e32 v38, 16, v168
	v_and_b32_e32 v39, 0xffff0000, v168
	v_lshlrev_b32_e32 v36, 16, v169
	v_and_b32_e32 v37, 0xffff0000, v169
	v_pk_add_f32 v[24:25], v[24:25], v[26:27]
	v_pk_add_f32 v[26:27], v[30:31], v[28:29]
	v_lshlrev_b32_e32 v28, 16, v176
	v_and_b32_e32 v29, 0xffff0000, v176
	v_lshlrev_b32_e32 v30, 16, v177
	v_and_b32_e32 v31, 0xffff0000, v177
	v_sub_f32_e32 v37, v37, v185
	v_sub_f32_e32 v36, v36, v185
	v_sub_f32_e32 v39, v39, v185
	v_sub_f32_e32 v38, v38, v185
	v_pk_fma_f32 v[22:23], v[184:185], v[28:29], v[22:23] op_sel_hi:[0,1,1]
	v_pk_fma_f32 v[16:17], v[184:185], v[30:31], v[16:17] op_sel_hi:[0,1,1]
	v_lshlrev_b32_e32 v28, 16, v172
	v_and_b32_e32 v29, 0xffff0000, v172
	v_lshlrev_b32_e32 v30, 16, v173
	v_and_b32_e32 v31, 0xffff0000, v173
	v_pk_mul_f32 v[38:39], v[38:39], v[214:215] op_sel_hi:[1,0]
	v_pk_mul_f32 v[36:37], v[36:37], v[214:215] op_sel_hi:[1,0]
	s_waitcnt vmcnt(2)
	v_pk_mul_f32 v[14:15], v[14:15], s[8:9] op_sel_hi:[1,0]
	v_pk_mul_f32 v[12:13], v[12:13], s[8:9] op_sel_hi:[1,0]
	v_pk_fma_f32 v[10:11], v[36:37], v[10:11], v[14:15]
	v_pk_fma_f32 v[12:13], v[38:39], v[8:9], v[12:13]
	v_pk_mul_f32 v[8:9], v[188:189], v[30:31] op_sel_hi:[0,1]
	v_pk_mul_f32 v[14:15], v[188:189], v[28:29] op_sel_hi:[0,1]
	v_lshlrev_b32_e32 v30, 16, v162
	v_and_b32_e32 v31, 0xffff0000, v162
	v_lshlrev_b32_e32 v28, 16, v163
	v_and_b32_e32 v29, 0xffff0000, v163
	v_pk_add_f32 v[16:17], v[16:17], v[18:19]
	v_pk_add_f32 v[18:19], v[22:23], v[20:21]
	v_lshlrev_b32_e32 v20, 16, v170
	v_and_b32_e32 v21, 0xffff0000, v170
	v_lshlrev_b32_e32 v22, 16, v171
	v_and_b32_e32 v23, 0xffff0000, v171
	v_sub_f32_e32 v29, v29, v185
	v_sub_f32_e32 v28, v28, v185
	v_sub_f32_e32 v31, v31, v185
	v_sub_f32_e32 v30, v30, v185
	v_pk_fma_f32 v[14:15], v[184:185], v[20:21], v[14:15] op_sel_hi:[0,1,1]
	v_pk_fma_f32 v[8:9], v[184:185], v[22:23], v[8:9] op_sel_hi:[0,1,1]
	v_lshlrev_b32_e32 v20, 16, v166
	v_and_b32_e32 v21, 0xffff0000, v166
	v_lshlrev_b32_e32 v22, 16, v167
	v_and_b32_e32 v23, 0xffff0000, v167
	v_pk_mul_f32 v[30:31], v[30:31], v[214:215] op_sel_hi:[1,0]
	v_pk_mul_f32 v[28:29], v[28:29], v[214:215] op_sel_hi:[1,0]
	s_waitcnt vmcnt(0)
	v_pk_mul_f32 v[6:7], v[6:7], s[8:9] op_sel_hi:[1,0]
	v_pk_mul_f32 v[4:5], v[4:5], s[8:9] op_sel_hi:[1,0]
	v_pk_add_f32 v[8:9], v[8:9], v[10:11]
	v_pk_add_f32 v[10:11], v[14:15], v[12:13]
	v_lshlrev_b32_e32 v12, 16, v164
	v_and_b32_e32 v13, 0xffff0000, v164
	v_lshlrev_b32_e32 v14, 16, v165
	v_and_b32_e32 v15, 0xffff0000, v165
	v_pk_fma_f32 v[2:3], v[28:29], v[2:3], v[6:7]
	v_pk_fma_f32 v[4:5], v[30:31], v[0:1], v[4:5]
	v_pk_mul_f32 v[0:1], v[188:189], v[22:23] op_sel_hi:[0,1]
	v_pk_mul_f32 v[6:7], v[188:189], v[20:21] op_sel_hi:[0,1]
	v_pk_fma_f32 v[6:7], v[184:185], v[12:13], v[6:7] op_sel_hi:[0,1,1]
	v_pk_fma_f32 v[0:1], v[184:185], v[14:15], v[0:1] op_sel_hi:[0,1,1]
	v_pk_add_f32 v[0:1], v[0:1], v[2:3]
	v_pk_add_f32 v[2:3], v[6:7], v[4:5]
	v_mov_b32_e32 v4, v58
	v_mov_b32_e32 v5, v50
	v_mov_b32_e32 v6, v59
	v_mov_b32_e32 v7, v51
	v_pk_add_f32 v[4:5], v[4:5], v[6:7]
	v_mov_b32_e32 v6, v56
	v_mov_b32_e32 v7, v48
	v_mov_b32_e32 v12, v57
	v_mov_b32_e32 v13, v49
	v_pk_add_f32 v[6:7], v[6:7], v[12:13]
	v_mov_b32_e32 v12, v42
	v_pk_add_f32 v[4:5], v[4:5], v[6:7]
	v_pk_mov_b32 v[6:7], v[42:43], v[40:41] op_sel:[1,0]
	v_mov_b32_e32 v13, v41
	v_pk_add_f32 v[6:7], v[6:7], v[12:13]
	v_add_f32_e32 v4, 0, v4
	v_pk_add_f32 v[6:7], v[6:7], v[6:7] op_sel:[0,1] op_sel_hi:[1,0]
	v_add_f32_e32 v4, v4, v5
	v_add_f32_e32 v12, v34, v35
	v_add_f32_e32 v14, v32, v33
	v_mov_b32_e32 v5, v26
	v_mov_b32_e32 v7, v27
	v_mov_b32_e32 v13, v24
	v_mov_b32_e32 v15, v25
	v_pk_add_f32 v[4:5], v[4:5], v[6:7]
	v_pk_add_f32 v[6:7], v[12:13], v[14:15]
	v_mov_b32_e32 v12, v18
	v_pk_add_f32 v[4:5], v[4:5], v[6:7]
	v_pk_mov_b32 v[6:7], v[18:19], v[16:17] op_sel:[1,0]
	v_mov_b32_e32 v13, v17
	v_pk_add_f32 v[6:7], v[6:7], v[12:13]
	v_pk_add_f32 v[4:5], v[4:5], v[4:5] op_sel:[0,1] op_sel_hi:[1,0]
	v_pk_add_f32 v[6:7], v[6:7], v[6:7] op_sel:[0,1] op_sel_hi:[1,0]
	v_add_f32_e32 v12, v10, v11
; __device__ __forceinline__ float dpp_row_sum(float x) {
;     x += __int_as_float(__builtin_amdgcn_mov_dpp(__float_as_int(x), 0xB1, 0xF, 0xF, true));
;     x += __int_as_float(__builtin_amdgcn_mov_dpp(__float_as_int(x), 0x4E, 0xF, 0xF, true));
;     x += __int_as_float(__builtin_amdgcn_mov_dpp(__float_as_int(x), 0x141, 0xF, 0xF, true));
;     x += __int_as_float(__builtin_amdgcn_mov_dpp(__float_as_int(x), 0x140, 0xF, 0xF, true));
;     return x; }
; __device__ __forceinline__ float wave_sum(float v) { v = dpp_row_sum(v); const int b = __float_as_int(v);
;     return (__int_as_float(__builtin_amdgcn_readlane(b, 0)) + __int_as_float(__builtin_amdgcn_readlane(b, 16))) + (__int_as_float(__builtin_amdgcn_readlane(b, 32)) + __int_as_float(__builtin_amdgcn_readlane(b, 48))); }
; __device__ __forceinline__ void ln_row(f32x4 (&v)[8], const float* g, const float* b, int lane) {
;     ...
;     const float mean = wave_sum(s) * (1.0f / DM); float q = 0.f;
; #pragma unroll
;     for (int j = 0; j < 8; ++j) { const f32x4 d = v[j] - mean; q += (d[0] * d[0] + d[1] * d[1]) + (d[2] * d[2] + d[3] * d[3]); }
;     const float rstd = rsqrtf(wave_sum(q) * (1.0f / DM) + 1e-5f);
; #pragma unroll
;     for (int j = 0; j < 8; ++j) { const f32x4 gg = *(const f32x4*)(g + j * 256 + lane * 4), bb = *(const f32x4*)(b + j * 256 + lane * 4); v[j] = (v[j] - mean) * rstd * gg + bb; }
	v_add_f32_e32 v14, v8, v9
	v_mov_b32_e32 v5, v2
	v_mov_b32_e32 v7, v3
	v_mov_b32_e32 v13, v0
	v_mov_b32_e32 v15, v1
	v_pk_add_f32 v[4:5], v[4:5], v[6:7]
	v_pk_add_f32 v[6:7], v[12:13], v[14:15]
	v_lshl_add_u64 v[112:113], v[112:113], 0, s[2:3]
	v_pk_add_f32 v[4:5], v[4:5], v[6:7]
	v_mov_b64_e32 v[202:203], v[116:117]
	v_add_f32_e32 v4, v4, v5
	v_mov_b64_e32 v[208:209], v[114:115]
	v_mov_b64_e32 v[204:205], v[124:125]
	v_add_f32_dpp v4, v4, v4 quad_perm:[1,0,3,2] row_mask:0xf bank_mask:0xf bound_ctrl:1
	v_mov_b64_e32 v[210:211], v[122:123]
	v_mov_b64_e32 v[206:207], v[130:131]
	v_add_f32_dpp v4, v4, v4 quad_perm:[2,3,0,1] row_mask:0xf bank_mask:0xf bound_ctrl:1
	v_mov_b64_e32 v[212:213], v[134:135]
	s_nop 0
	v_add_f32_dpp v4, v4, v4 row_half_mirror row_mask:0xf bank_mask:0xf bound_ctrl:1
	s_nop 1
	v_add_f32_dpp v4, v4, v4 row_mirror row_mask:0xf bank_mask:0xf bound_ctrl:1
	s_nop 0
	v_readlane_b32 s17, v4, 16
	v_readlane_b32 s18, v4, 48
	v_readlane_b32 s10, v4, 0
	v_readlane_b32 s11, v4, 32
	v_mov_b32_e32 v4, s17
	v_mov_b32_e32 v5, s18
	v_pk_add_f32 v[4:5], s[10:11], v[4:5]
	s_nop 0
	v_add_f32_e32 v111, v4, v5
	v_fmamk_f32 v59, v111, 0xba000000, v59
	v_fmamk_f32 v51, v111, 0xba000000, v51
	v_fmamk_f32 v57, v111, 0xba000000, v57
	v_fmac_f32_e32 v58, 0xba000000, v111
	v_fmamk_f32 v49, v111, 0xba000000, v49
	v_fmac_f32_e32 v50, 0xba000000, v111
	v_mov_b32_e32 v6, v59
	v_mov_b32_e32 v7, v51
	v_fmac_f32_e32 v56, 0xba000000, v111
	v_fmac_f32_e32 v48, 0xba000000, v111
	v_mov_b32_e32 v4, v58
	v_mov_b32_e32 v5, v50
	v_pk_mul_f32 v[6:7], v[6:7], v[6:7]
	v_mov_b32_e32 v12, v57
	v_mov_b32_e32 v13, v49
	v_pk_fma_f32 v[4:5], v[4:5], v[4:5], v[6:7]
	v_mov_b32_e32 v6, v56
	v_mov_b32_e32 v7, v48
	v_pk_mul_f32 v[12:13], v[12:13], v[12:13]
	v_fmamk_f32 v43, v111, 0xba000000, v43
	v_pk_fma_f32 v[6:7], v[6:7], v[6:7], v[12:13]
	v_fmac_f32_e32 v42, 0xba000000, v111
	v_pk_add_f32 v[4:5], v[4:5], v[6:7]
	v_fmamk_f32 v41, v111, 0xba000000, v41
	v_fmac_f32_e32 v40, 0xba000000, v111
	v_pk_add_f32 v[170:171], v[4:5], v[4:5] op_sel_hi:[0,1]
	v_pk_mul_f32 v[4:5], v[40:41], v[40:41]
	v_pk_mul_f32 v[6:7], v[42:43], v[42:43]
	v_fmac_f32_e32 v34, 0xba000000, v111
	v_pk_mov_b32 v[12:13], v[6:7], v[4:5] op_sel:[1,0]
	v_mov_b32_e32 v7, v5
	v_pk_add_f32 v[4:5], v[12:13], v[6:7]
	v_fmamk_f32 v35, v111, 0xba000000, v35
	v_pk_add_f32 v[172:173], v[4:5], v[4:5] op_sel_hi:[0,1]
	v_fmac_f32_e32 v32, 0xba000000, v111
	v_mul_f32_e32 v4, v34, v34
	v_fmamk_f32 v33, v111, 0xba000000, v33
	v_pk_fma_f32 v[162:163], v[34:35], v[34:35], v[4:5] op_sel_hi:[1,1,0]
	v_mul_f32_e32 v4, v32, v32
	v_pk_fma_f32 v[164:165], v[32:33], v[32:33], v[4:5] op_sel_hi:[1,1,0]
	v_fmamk_f32 v25, v111, 0xba000000, v25
	global_load_dwordx4 v[4:7], v[88:89], off
	global_load_dwordx4 v[12:15], v[90:91], off
	v_fmac_f32_e32 v24, 0xba000000, v111
	v_fmamk_f32 v27, v111, 0xba000000, v27
	v_fmac_f32_e32 v26, 0xba000000, v111
	global_load_dwordx4 v[20:23], v[88:89], off offset:1024
	global_load_dwordx4 v[28:31], v[90:91], off offset:1024
	v_mul_f32_e32 v162, v26, v26
	v_mul_f32_e32 v164, v27, v27
	v_mul_f32_e32 v172, v24, v24
	v_mul_f32_e32 v170, v25, v25
	global_load_dwordx4 v[36:39], v[88:89], off offset:2048
	global_load_dwordx4 v[44:47], v[90:91], off offset:2048
	global_load_dwordx4 v[52:55], v[88:89], off offset:3072
	global_load_dwordx4 v[60:63], v[90:91], off offset:3072
	v_pk_add_f32 v[174:175], v[162:163], v[164:165]
	global_load_dwordx4 v[162:165], v[92:93], off
	global_load_dwordx4 v[166:169], v[94:95], off
	v_pk_add_f32 v[170:171], v[172:173], v[170:171]
	v_fmamk_f32 v19, v111, 0xba000000, v19
	v_pk_add_f32 v[178:179], v[174:175], v[170:171]
	global_load_dwordx4 v[170:173], v[96:97], off
	global_load_dwordx4 v[174:177], v[98:99], off
	v_pk_add_f32 v[194:195], v[178:179], v[178:179] op_sel_hi:[0,1]
	global_load_dwordx4 v[178:181], v[100:101], off
	global_load_dwordx4 v[182:185], v[102:103], off
	global_load_dwordx4 v[186:189], v[104:105], off
	global_load_dwordx4 v[190:193], v[106:107], off
	v_fmac_f32_e32 v18, 0xba000000, v111
	v_fmamk_f32 v17, v111, 0xba000000, v17
	v_fmac_f32_e32 v16, 0xba000000, v111
	v_pk_mul_f32 v[196:197], v[16:17], v[16:17]
	v_pk_mul_f32 v[198:199], v[18:19], v[18:19]
	v_fmac_f32_e32 v10, 0xba000000, v111
	v_pk_mov_b32 v[200:201], v[198:199], v[196:197] op_sel:[1,0]
	v_mov_b32_e32 v199, v197
	v_fmamk_f32 v11, v111, 0xba000000, v11
	v_fmac_f32_e32 v8, 0xba000000, v111
	v_mul_f32_e32 v194, v10, v10
	v_pk_add_f32 v[196:197], v[200:201], v[198:199]
	v_fmamk_f32 v9, v111, 0xba000000, v9
	v_pk_fma_f32 v[198:199], v[10:11], v[10:11], v[194:195] op_sel_hi:[1,1,0]
	v_mul_f32_e32 v194, v8, v8
	v_pk_add_f32 v[196:197], v[196:197], v[196:197] op_sel_hi:[0,1]
	v_pk_fma_f32 v[200:201], v[8:9], v[8:9], v[194:195] op_sel_hi:[1,1,0]
	v_fmamk_f32 v1, v111, 0xba000000, v1
	v_fmac_f32_e32 v0, 0xba000000, v111
	v_fmamk_f32 v3, v111, 0xba000000, v3
	v_fmac_f32_e32 v2, 0xba000000, v111
	v_mul_f32_e32 v198, v2, v2
	v_mul_f32_e32 v200, v3, v3
	v_mul_f32_e32 v196, v0, v0
	v_mul_f32_e32 v194, v1, v1
	v_pk_add_f32 v[198:199], v[198:199], v[200:201]
	v_pk_add_f32 v[194:195], v[196:197], v[194:195]
	v_mov_b64_e32 v[196:197], v[118:119]
	v_pk_add_f32 v[194:195], v[198:199], v[194:195]
	v_mov_b64_e32 v[198:199], v[126:127]
	v_add_f32_e32 v111, v194, v195
	v_mov_b64_e32 v[200:201], v[132:133]
	s_nop 0
	v_add_f32_dpp v111, v111, v111 quad_perm:[1,0,3,2] row_mask:0xf bank_mask:0xf bound_ctrl:1
	s_nop 1
	v_add_f32_dpp v111, v111, v111 quad_perm:[2,3,0,1] row_mask:0xf bank_mask:0xf bound_ctrl:1
	s_nop 1
	v_add_f32_dpp v111, v111, v111 row_half_mirror row_mask:0xf bank_mask:0xf bound_ctrl:1
	s_nop 1
	v_add_f32_dpp v111, v111, v111 row_mirror row_mask:0xf bank_mask:0xf bound_ctrl:1
	s_nop 0
	v_readlane_b32 s17, v111, 16
	v_readlane_b32 s18, v111, 48
	v_readlane_b32 s10, v111, 0
	v_readlane_b32 s11, v111, 32
	v_mov_b32_e32 v194, s17
	v_mov_b32_e32 v195, s18
	v_pk_add_f32 v[194:195], s[10:11], v[194:195]
	s_nop 0
	v_add_f32_e32 v111, v194, v195
	v_fmamk_f32 v111, v111, 0x3a000000, v65
	v_mul_f32_e32 v194, 0x4b800000, v111
	v_cmp_gt_f32_e32 vcc, s16, v111
	s_nop 1
	v_cndmask_b32_e32 v111, v111, v194, vcc
	v_rsq_f32_e32 v111, v111
	s_nop 0
	v_mul_f32_e32 v194, 0x45800000, v111
	v_cndmask_b32_e32 v194, v111, v194, vcc
	v_pk_mul_f32 v[56:57], v[56:57], v[194:195] op_sel_hi:[1,0]
	v_pk_mul_f32 v[24:25], v[24:25], v[194:195] op_sel_hi:[1,0]
	s_waitcnt vmcnt(14)
; __device__ __forceinline__ void ln_row(f32x4 (&v)[8], const float* g, const float* b, int lane) {
;     ...
;     const float rstd = rsqrtf(wave_sum(q) * (1.0f / DM) + 1e-5f);
; #pragma unroll
;     for (int j = 0; j < 8; ++j) { const f32x4 gg = *(const f32x4*)(g + j * 256 + lane * 4), bb = *(const f32x4*)(b + j * 256 + lane * 4); v[j] = (v[j] - mean) * rstd * gg + bb; }
; __device__ __forceinline__ void ph_ln3(const Params& p) {
;     ...
;         ln_row(v, p.ln3_g, p.ln3_b, lane);
; #pragma unroll
;         for (int j = 0; j < 8; ++j) *(f32x4*)(p.out + (size_t)row * DM + j * 256 + lane * 4) = v[j];
;     }
	v_pk_fma_f32 v[6:7], v[6:7], v[56:57], v[14:15]
	v_pk_mul_f32 v[14:15], v[48:49], v[194:195] op_sel_hi:[1,0]
	v_pk_mul_f32 v[58:59], v[58:59], v[194:195] op_sel_hi:[1,0]
	s_waitcnt vmcnt(12)
	v_pk_fma_f32 v[14:15], v[22:23], v[14:15], v[30:31]
	v_pk_mul_f32 v[30:31], v[32:33], v[194:195] op_sel_hi:[1,0]
	v_pk_mul_f32 v[32:33], v[26:27], v[194:195] op_sel_hi:[1,0]
	s_waitcnt vmcnt(6)
	v_pk_fma_f32 v[26:27], v[164:165], v[24:25], v[168:169]
	v_pk_fma_f32 v[24:25], v[162:163], v[32:33], v[166:167]
	v_pk_mul_f32 v[32:33], v[18:19], v[194:195] op_sel_hi:[1,0]
	v_pk_mul_f32 v[16:17], v[16:17], v[194:195] op_sel_hi:[1,0]
	v_pk_fma_f32 v[4:5], v[4:5], v[58:59], v[12:13]
	v_pk_mul_f32 v[12:13], v[50:51], v[194:195] op_sel_hi:[1,0]
	s_waitcnt vmcnt(4)
	v_pk_fma_f32 v[18:19], v[172:173], v[16:17], v[176:177]
	v_pk_fma_f32 v[16:17], v[170:171], v[32:33], v[174:175]
	v_pk_mul_f32 v[32:33], v[10:11], v[194:195] op_sel_hi:[1,0]
	v_pk_mul_f32 v[8:9], v[8:9], v[194:195] op_sel_hi:[1,0]
	v_pk_fma_f32 v[12:13], v[20:21], v[12:13], v[28:29]
	v_pk_mul_f32 v[20:21], v[42:43], v[194:195] op_sel_hi:[1,0]
	v_pk_mul_f32 v[22:23], v[40:41], v[194:195] op_sel_hi:[1,0]
	v_pk_mul_f32 v[28:29], v[34:35], v[194:195] op_sel_hi:[1,0]
	s_waitcnt vmcnt(2)
	v_pk_fma_f32 v[10:11], v[180:181], v[8:9], v[184:185]
	v_pk_fma_f32 v[8:9], v[178:179], v[32:33], v[182:183]
	v_pk_mul_f32 v[32:33], v[2:3], v[194:195] op_sel_hi:[1,0]
	v_pk_mul_f32 v[0:1], v[0:1], v[194:195] op_sel_hi:[1,0]
	v_pk_fma_f32 v[22:23], v[38:39], v[22:23], v[46:47]
	v_pk_fma_f32 v[20:21], v[36:37], v[20:21], v[44:45]
	v_pk_fma_f32 v[30:31], v[54:55], v[30:31], v[62:63]
	v_pk_fma_f32 v[28:29], v[52:53], v[28:29], v[60:61]
	s_waitcnt vmcnt(0)
	v_pk_fma_f32 v[2:3], v[0:1], v[188:189], v[192:193]
	v_pk_fma_f32 v[0:1], v[32:33], v[186:187], v[190:191]
	global_store_dwordx4 v[108:109], v[4:7], off offset:-4096 nt
	global_store_dwordx4 v[108:109], v[12:15], off offset:-3072 nt
	global_store_dwordx4 v[108:109], v[20:23], off offset:-2048 nt
	global_store_dwordx4 v[108:109], v[28:31], off offset:-1024 nt
	global_store_dwordx4 v[108:109], v[24:27], off nt
	global_store_dwordx4 v[108:109], v[16:19], off offset:1024 nt
	global_store_dwordx4 v[108:109], v[8:11], off offset:2048 nt
	global_store_dwordx4 v[108:109], v[0:3], off offset:3072 nt
	v_lshl_add_u64 v[108:109], v[108:109], 0, s[4:5]
	v_mov_b64_e32 v[162:163], v[144:145]
	v_mov_b64_e32 v[168:169], v[142:143]
	v_mov_b64_e32 v[174:175], v[140:141]
	v_mov_b64_e32 v[180:181], v[138:139]
	v_mov_b64_e32 v[190:191], v[120:121]
	v_mov_b64_e32 v[164:165], v[152:153]
	v_mov_b64_e32 v[170:171], v[150:151]
	v_mov_b64_e32 v[176:177], v[148:149]
	v_mov_b64_e32 v[182:183], v[146:147]
	v_mov_b64_e32 v[192:193], v[128:129]
	v_mov_b64_e32 v[166:167], v[160:161]
	v_mov_b64_e32 v[172:173], v[158:159]
	v_mov_b64_e32 v[178:179], v[156:157]
	v_mov_b64_e32 v[186:187], v[154:155]
	v_mov_b64_e32 v[194:195], v[136:137]
	s_andn2_b64 exec, exec, s[6:7]
	s_cbranch_execz .LBB0_1514
